# attention hot loops: first batch of PV ds_read_b64_tr_b16 hoisted into the QK^T tail right after the last use of each destination (counted lgkmcnt waits bumped accordingly)
# baseline (speedup 1.0000x reference)
.Lcw_a_done:
	s_mov_b32 s1, s97
	s_mov_b32 m0, s86
	s_add_i32 s5, s0, 0xffff2000
	ds_read_b128 v[0:3], v190 offset:32768
	ds_read_b128 v[112:115], v190 offset:40960
	buffer_load_dwordx4 v191, s[68:71], s5 offen lds
	ds_read_b128 v[4:7], v189 offset:32768
	ds_read_b128 v[116:119], v189 offset:40960
	s_add_i32 s6, s0, 0xffff4000
	s_mov_b32 m0, s85
	s_waitcnt lgkmcnt(3)
	v_mfma_f32_32x32x16_f16 v[80:95], v[0:3], v[156:159], -0.5
	s_add_i32 s7, s0, 0xffff6000
	buffer_load_dwordx4 v191, s[68:71], s6 offen lds
	s_waitcnt lgkmcnt(1)
	v_mfma_f32_32x32x16_f16 v[80:95], v[4:7], v[152:155], v[80:95]
	v_mfma_f32_32x32x16_f16 v[0:15], v[112:115], v[156:159], -0.5
	ds_read_b128 v[112:115], v188 offset:32768
	s_mov_b32 m0, s84
	s_add_i32 s9, s0, 0xffff8000
	s_add_i32 s10, s0, 0xfffea000
	v_exp_f32_e32 v182, v100
	v_exp_f32_e32 v183, v101
	s_waitcnt lgkmcnt(1)
	v_mfma_f32_32x32x16_f16 v[0:15], v[116:119], v[152:155], v[0:15]
	ds_read_b128 v[116:119], v188 offset:40960
	buffer_load_dwordx4 v191, s[68:71], s7 offen lds
	s_mov_b32 m0, s83
	v_exp_f32_e32 v192, v106
	v_exp_f32_e32 v193, v107
	v_exp_f32_e32 v194, v108
	v_exp_f32_e32 v111, v111
	s_waitcnt lgkmcnt(1)
	v_mfma_f32_32x32x16_f16 v[80:95], v[112:115], v[148:151], v[80:95]
	ds_read_b128 v[112:115], v187 offset:32768
	ds_read_b128 v[120:123], v187 offset:40960
	buffer_load_dwordx4 v191, s[68:71], s9 offen lds
	s_mov_b32 m0, s90
	ds_read_b128 v[124:127], v190 offset:32896
	ds_read_b128 v[162:165], v190 offset:41088
	buffer_load_dwordx4 v186, s[72:75], s10 offen lds
	s_add_i32 s10, s0, 0xfffec000
	s_mov_b32 m0, s89
	s_waitcnt lgkmcnt(4)
	v_mfma_f32_32x32x16_f16 v[0:15], v[116:119], v[148:151], v[0:15]
	ds_read_b128 v[116:119], v189 offset:32896
	ds_read_b128 v[166:169], v189 offset:41088
	buffer_load_dwordx4 v186, s[72:75], s10 offen lds
	s_add_i32 s10, s0, 0xfffee000
	s_mov_b32 m0, s88
	v_cvt_pk_f16_f32 v100, v218, v219
	v_cvt_pk_f16_f32 v101, v220, v221
	v_cvt_pk_f16_f32 v106, v182, v183
	s_waitcnt lgkmcnt(5)
	v_mfma_f32_32x32x16_f16 v[80:95], v[112:115], v[144:147], v[80:95]
	ds_read_b128 v[112:115], v188 offset:32896
	ds_read_b128 v[170:173], v188 offset:41088
	buffer_load_dwordx4 v186, s[72:75], s10 offen lds
	s_add_i32 s10, s0, 0xffff0000
	s_mov_b32 m0, s87
	ds_read_b128 v[174:177], v187 offset:32896
	ds_read_b128 v[178:181], v187 offset:41088
	buffer_load_dwordx4 v186, s[72:75], s10 offen lds
	s_waitcnt lgkmcnt(8)
	v_mfma_f32_32x32x16_f16 v[0:15], v[120:123], v[144:147], v[0:15]
	v_exp_f32_e32 v120, v96
	v_add_f32_e32 v96, 0, v210
	v_add_f32_e32 v96, v211, v96
	v_add_f32_e32 v96, v212, v96
	v_add_f32_e32 v96, v213, v96
	v_add_f32_e32 v96, v214, v96
	v_add_f32_e32 v96, v215, v96
	s_waitcnt lgkmcnt(7)
	v_mfma_f32_32x32x16_f16 v[80:95], v[124:127], v[140:143], v[80:95]
	v_add_f32_e32 v96, v216, v96
	v_add_f32_e32 v96, v217, v96
	v_add_f32_e32 v96, v218, v96
	v_add_f32_e32 v96, v219, v96
	v_add_f32_e32 v96, v220, v96
	v_add_f32_e32 v96, v221, v96
	v_add_f32_e32 v96, v222, v96
	v_exp_f32_e32 v121, v97
	s_waitcnt lgkmcnt(6)
	v_mfma_f32_32x32x16_f16 v[0:15], v[162:165], v[140:143], v[0:15]
	v_add_f32_e32 v96, v223, v96
	v_exp_f32_e32 v122, v98
	v_add_f32_e32 v96, v224, v96
	v_exp_f32_e32 v123, v99
	v_add_f32_e32 v96, v225, v96
	v_add_f32_e32 v96, v120, v96
	v_add_f32_e32 v96, v121, v96
	s_waitcnt lgkmcnt(5)
	v_mfma_f32_32x32x16_f16 v[80:95], v[116:119], v[136:139], v[80:95]
	v_exp_f32_e32 v124, v102
	v_add_f32_e32 v96, v122, v96
	v_exp_f32_e32 v125, v103
	v_add_f32_e32 v96, v123, v96
	v_exp_f32_e32 v126, v104
	v_add_f32_e32 v96, v182, v96
	v_exp_f32_e32 v127, v105
	s_waitcnt lgkmcnt(4)
	v_mfma_f32_32x32x16_f16 v[0:15], v[166:169], v[136:139], v[0:15]
	v_add_f32_e32 v96, v183, v96
	v_add_f32_e32 v96, v124, v96
	v_add_f32_e32 v96, v125, v96
	v_add_f32_e32 v96, v126, v96
	v_exp_f32_e32 v162, v109
	v_add_f32_e32 v96, v127, v96
	v_exp_f32_e32 v163, v110
	s_waitcnt lgkmcnt(3)
	v_mfma_f32_32x32x16_f16 v[80:95], v[112:115], v[132:135], v[80:95]
	ds_read_b64_tr_b16 v[112:113], v184 offset:0
	ds_read_b64_tr_b16 v[114:115], v184 offset:0x800
	ds_read_b64_tr_b16 v[116:117], v184 offset:0x1000
	ds_read_b64_tr_b16 v[118:119], v184 offset:0x1800
	v_add_f32_e32 v96, v192, v96
	v_add_f32_e32 v96, v193, v96
	v_add_f32_e32 v96, v194, v96
	v_add_f32_e32 v96, v162, v96
	v_add_f32_e32 v96, v163, v96
	v_add_f32_e32 v96, v111, v96
	v_mov_b32_e32 v97, v96
	s_waitcnt lgkmcnt(6)
	v_mfma_f32_32x32x16_f16 v[0:15], v[170:173], v[132:135], v[0:15]
	v_permlane32_swap_b32_e32 v96, v97
	v_add_f32_e32 v96, v96, v97
	v_add_f32_e32 v185, v185, v96
	v_cvt_pk_f16_f32 v96, v210, v211
	v_cvt_pk_f16_f32 v97, v212, v213
	v_cvt_pk_f16_f32 v98, v214, v215
	s_waitcnt lgkmcnt(5)
	v_mfma_f32_32x32x16_f16 v[80:95], v[174:177], v[128:131], v[80:95]
	v_cvt_pk_f16_f32 v99, v216, v217
	v_cvt_pk_f16_f32 v102, v222, v223
	v_cvt_pk_f16_f32 v103, v224, v225
	v_cvt_pk_f16_f32 v104, v120, v121
	ds_read_b64_tr_b16 v[120:121], v184 offset:0x2000
	v_cvt_pk_f16_f32 v105, v122, v123
	ds_read_b64_tr_b16 v[122:123], v184 offset:0x2800
	v_cvt_pk_f16_f32 v107, v124, v125
	ds_read_b64_tr_b16 v[124:125], v184 offset:0x3000
	v_cvt_pk_f16_f32 v108, v126, v127
	ds_read_b64_tr_b16 v[126:127], v184 offset:0x3800
	v_cvt_pk_f16_f32 v109, v192, v193
	v_cvt_pk_f16_f32 v110, v194, v162
	v_cvt_pk_f16_f32 v111, v163, v111
	v_permlane32_swap_b32_e32 v96, v98
	v_permlane32_swap_b32_e32 v97, v99
	v_permlane32_swap_b32_e32 v100, v102
	v_permlane32_swap_b32_e32 v101, v103
	v_permlane32_swap_b32_e32 v104, v106
	v_permlane32_swap_b32_e32 v105, v107
	v_permlane32_swap_b32_e32 v108, v110
	v_permlane32_swap_b32_e32 v109, v111
	s_waitcnt lgkmcnt(8)
	v_mfma_f32_32x32x16_f16 v[0:15], v[178:181], v[128:131], v[0:15]
	s_waitcnt lgkmcnt(0)
	s_nop 0
	v_mfma_f32_32x32x16_f16 v[64:79], v[96:99], v[112:115], v[64:79]
	v_exp_f32_e32 v208, v80
	v_exp_f32_e32 v192, v81
	ds_read_b64_tr_b16 v[80:81], v184 offset:0x200
	v_exp_f32_e32 v193, v82
	v_exp_f32_e32 v194, v83
	ds_read_b64_tr_b16 v[82:83], v184 offset:0xa00
	ds_read_b64_tr_b16 v[112:113], v184 offset:0x1200
	v_mfma_f32_32x32x16_f16 v[64:79], v[100:103], v[116:119], v[64:79]
	ds_read_b64_tr_b16 v[114:115], v184 offset:0x1a00
	ds_read_b64_tr_b16 v[116:117], v184 offset:0x2200
	ds_read_b64_tr_b16 v[118:119], v184 offset:0x2a00
	v_mfma_f32_32x32x16_f16 v[64:79], v[104:107], v[120:123], v[64:79]
	ds_read_b64_tr_b16 v[120:121], v184 offset:0x3200
	ds_read_b64_tr_b16 v[122:123], v184 offset:0x3a00
	v_mfma_f32_32x32x16_f16 v[64:79], v[108:111], v[124:127], v[64:79]
	s_waitcnt lgkmcnt(0)
	v_mfma_f32_32x32x16_f16 v[48:63], v[96:99], v[80:83], v[48:63]
	ds_read_b64_tr_b16 v[80:81], v184 offset:0x400
	ds_read_b64_tr_b16 v[82:83], v184 offset:0xc00
	v_exp_f32_e32 v195, v84
	v_exp_f32_e32 v196, v85
	ds_read_b64_tr_b16 v[84:85], v184 offset:0x1400
	v_exp_f32_e32 v197, v86
	v_exp_f32_e32 v198, v87
	v_mfma_f32_32x32x16_f16 v[48:63], v[100:103], v[112:115], v[48:63]
	ds_read_b64_tr_b16 v[86:87], v184 offset:0x1c00
	ds_read_b64_tr_b16 v[112:113], v184 offset:0x2400
	ds_read_b64_tr_b16 v[114:115], v184 offset:0x2c00
	v_mfma_f32_32x32x16_f16 v[48:63], v[104:107], v[116:119], v[48:63]
	ds_read_b64_tr_b16 v[116:117], v184 offset:0x3400
	ds_read_b64_tr_b16 v[118:119], v184 offset:0x3c00
	v_mfma_f32_32x32x16_f16 v[48:63], v[108:111], v[120:123], v[48:63]
	s_waitcnt lgkmcnt(0)
	v_mfma_f32_32x32x16_f16 v[32:47], v[96:99], v[80:83], v[32:47]
	ds_read_b64_tr_b16 v[80:81], v184 offset:0x600
	ds_read_b64_tr_b16 v[82:83], v184 offset:0xe00
	v_exp_f32_e32 v199, v88
	v_exp_f32_e32 v200, v89
	v_exp_f32_e32 v201, v90
	v_exp_f32_e32 v202, v91
	v_mfma_f32_32x32x16_f16 v[32:47], v[100:103], v[84:87], v[32:47]
	ds_read_b64_tr_b16 v[84:85], v184 offset:0x1600
	ds_read_b64_tr_b16 v[86:87], v184 offset:0x1e00
	ds_read_b64_tr_b16 v[88:89], v184 offset:0x2600
	ds_read_b64_tr_b16 v[90:91], v184 offset:0x2e00
	v_mfma_f32_32x32x16_f16 v[32:47], v[104:107], v[112:115], v[32:47]
	ds_read_b64_tr_b16 v[112:113], v184 offset:0x3600
	ds_read_b64_tr_b16 v[114:115], v184 offset:0x3e00
	v_mfma_f32_32x32x16_f16 v[32:47], v[108:111], v[116:119], v[32:47]
	s_waitcnt lgkmcnt(0)
	v_mfma_f32_32x32x16_f16 v[16:31], v[96:99], v[80:83], v[16:31]
	v_exp_f32_e32 v203, v92
	v_exp_f32_e32 v204, v93
	v_exp_f32_e32 v205, v94
	v_exp_f32_e32 v206, v95
	s_waitcnt vmcnt(0) lgkmcnt(0)
	s_barrier
	v_mfma_f32_32x32x16_f16 v[16:31], v[100:103], v[84:87], v[16:31]
	v_mfma_f32_32x32x16_f16 v[16:31], v[104:107], v[88:91], v[16:31]
	v_mfma_f32_32x32x16_f16 v[16:31], v[108:111], v[112:115], v[16:31]
	s_cmp_gt_u32 s100, 8
	s_cbranch_scc1 .Lcw_b_done
	s_cmp_eq_u32 s100, 0
	s_cbranch_scc1 .Lcw_b_load
	v_cvt_pk_f16_f32 v252, v252, v253
	v_cvt_pk_f16_f32 v253, v254, v255
	v_lshrrev_b32_e32 v254, 1, v191
	global_store_dwordx2 v254, v[252:253], s[60:61]
	s_add_u32 s60, s60, 0x1000
	s_addc_u32 s61, s61, 0
	s_cmp_eq_u32 s100, 8
	s_cbranch_scc1 .Lcw_b_inc

.Lcw_b_done:
	s_mov_b32 m0, s91
	s_add_i32 s10, s0, 0xffffa000
	ds_read_b128 v[80:83], v190
	ds_read_b128 v[84:87], v190 offset:8192
	buffer_load_dwordx4 v191, s[68:71], s10 offen lds
	ds_read_b128 v[88:91], v189
	ds_read_b128 v[92:95], v189 offset:8192
	s_add_i32 s10, s0, 0xffffc000
	s_mov_b32 m0, s92
	s_waitcnt lgkmcnt(3)
	v_mfma_f32_32x32x16_f16 v[112:127], v[80:83], v[156:159], -0.5
	s_waitcnt lgkmcnt(2)
	v_mfma_f32_32x32x16_f16 v[96:111], v[84:87], v[156:159], -0.5
	buffer_load_dwordx4 v191, s[68:71], s10 offen lds
	ds_read_b128 v[80:83], v188
	ds_read_b128 v[84:87], v188 offset:8192
	s_waitcnt lgkmcnt(3)
	v_mfma_f32_32x32x16_f16 v[112:127], v[88:91], v[152:155], v[112:127]
	s_add_i32 s10, s0, 0xffffe000
	s_mov_b32 m0, s93
	s_nop 0
	buffer_load_dwordx4 v191, s[68:71], s10 offen lds
	s_mov_b32 m0, s94
	s_waitcnt lgkmcnt(1)
	v_mfma_f32_32x32x16_f16 v[112:127], v[80:83], v[148:151], v[112:127]
	ds_read_b128 v[80:83], v187
	ds_read_b128 v[88:91], v187 offset:8192
	buffer_load_dwordx4 v191, s[68:71], s0 offen lds
	s_mov_b32 m0, s3
	v_mfma_f32_32x32x16_f16 v[96:111], v[92:95], v[152:155], v[96:111]
	ds_read_b128 v[92:95], v190 offset:128
	ds_read_b128 v[162:165], v190 offset:8320
	buffer_load_dwordx4 v186, s[72:75], s5 offen lds
	s_mov_b32 m0, s82
	ds_read_b128 v[166:169], v189 offset:128
	ds_read_b128 v[170:173], v189 offset:8320
	buffer_load_dwordx4 v186, s[72:75], s6 offen lds
	s_mov_b32 m0, s81
	ds_read_b128 v[174:177], v188 offset:128
	ds_read_b128 v[178:181], v188 offset:8320
	buffer_load_dwordx4 v186, s[72:75], s7 offen lds
	s_mov_b32 m0, s80
	ds_read_b128 v[210:213], v187 offset:128
	ds_read_b128 v[214:217], v187 offset:8320
	buffer_load_dwordx4 v186, s[72:75], s9 offen lds
	s_waitcnt lgkmcnt(10)
	v_mfma_f32_32x32x16_f16 v[96:111], v[84:87], v[148:151], v[96:111]
	v_exp_f32_e32 v84, v4
	v_exp_f32_e32 v85, v5
	v_exp_f32_e32 v86, v6
	v_exp_f32_e32 v87, v7
	v_cvt_pk_f16_f32 v4, v199, v200
	v_cvt_pk_f16_f32 v5, v201, v202
	v_cvt_pk_f16_f32 v6, v203, v204
	s_waitcnt lgkmcnt(8)
	v_mfma_f32_32x32x16_f16 v[96:111], v[88:91], v[144:147], v[96:111]
	v_exp_f32_e32 v88, v8
	v_exp_f32_e32 v89, v9
	v_exp_f32_e32 v90, v10
	v_exp_f32_e32 v91, v11
	v_cvt_pk_f16_f32 v7, v205, v206
	v_cvt_pk_f16_f32 v10, v84, v85
	v_cvt_pk_f16_f32 v11, v86, v87
	v_mfma_f32_32x32x16_f16 v[112:127], v[80:83], v[144:147], v[112:127]
	v_exp_f32_e32 v80, v0
	v_add_f32_e32 v0, 0, v208
	v_add_f32_e32 v0, v192, v0
	v_add_f32_e32 v0, v193, v0
	v_add_f32_e32 v0, v194, v0
	v_add_f32_e32 v0, v195, v0
	v_add_f32_e32 v0, v196, v0
	s_waitcnt lgkmcnt(6)
	v_mfma_f32_32x32x16_f16 v[96:111], v[162:165], v[140:143], v[96:111]
	ds_read_b64_tr_b16 v[162:163], v184 offset:0x8000
	ds_read_b64_tr_b16 v[164:165], v184 offset:0x8800
	v_add_f32_e32 v0, v197, v0
	v_add_f32_e32 v0, v198, v0
	v_add_f32_e32 v0, v199, v0
	v_add_f32_e32 v0, v200, v0
	v_add_f32_e32 v0, v201, v0
	v_add_f32_e32 v0, v202, v0
	v_add_f32_e32 v0, v203, v0
	v_mfma_f32_32x32x16_f16 v[112:127], v[92:95], v[140:143], v[112:127]
	v_exp_f32_e32 v81, v1
	v_add_f32_e32 v0, v204, v0
	v_exp_f32_e32 v82, v2
	v_add_f32_e32 v0, v205, v0
	v_exp_f32_e32 v83, v3
	v_add_f32_e32 v0, v206, v0
	v_add_f32_e32 v0, v80, v0
	s_waitcnt lgkmcnt(6)
	v_mfma_f32_32x32x16_f16 v[96:111], v[170:173], v[136:139], v[96:111]
	v_add_f32_e32 v0, v81, v0
	v_add_f32_e32 v0, v82, v0
	v_add_f32_e32 v0, v83, v0
	v_add_f32_e32 v0, v84, v0
	v_add_f32_e32 v0, v85, v0
	v_add_f32_e32 v0, v86, v0
	v_add_f32_e32 v0, v87, v0
	v_mfma_f32_32x32x16_f16 v[112:127], v[166:169], v[136:139], v[112:127]
	ds_read_b64_tr_b16 v[166:167], v184 offset:0x9000
	ds_read_b64_tr_b16 v[168:169], v184 offset:0x9800
	ds_read_b64_tr_b16 v[170:171], v184 offset:0xa000
	ds_read_b64_tr_b16 v[172:173], v184 offset:0xa800
	v_exp_f32_e32 v92, v12
	v_add_f32_e32 v0, v88, v0
	v_exp_f32_e32 v93, v13
	v_add_f32_e32 v0, v89, v0
	v_exp_f32_e32 v94, v14
	v_add_f32_e32 v0, v90, v0
	v_exp_f32_e32 v95, v15
	s_waitcnt lgkmcnt(8)
	v_mfma_f32_32x32x16_f16 v[96:111], v[178:181], v[132:135], v[96:111]
	v_add_f32_e32 v0, v91, v0
	v_add_f32_e32 v0, v92, v0
	v_add_f32_e32 v0, v93, v0
	v_add_f32_e32 v0, v94, v0
	v_add_f32_e32 v0, v95, v0
	v_mov_b32_e32 v1, v0
	s_nop 1
	v_permlane32_swap_b32_e32 v0, v1
	v_mfma_f32_32x32x16_f16 v[112:127], v[174:177], v[132:135], v[112:127]
	ds_read_b64_tr_b16 v[174:175], v184 offset:0xb000
	ds_read_b64_tr_b16 v[176:177], v184 offset:0xb800
	v_add_f32_e32 v0, v0, v1
	v_add_f32_e32 v185, v185, v0
	v_cvt_pk_f16_f32 v0, v208, v192
	v_cvt_pk_f16_f32 v1, v193, v194
	v_cvt_pk_f16_f32 v2, v195, v196
	v_cvt_pk_f16_f32 v3, v197, v198
	v_cvt_pk_f16_f32 v8, v80, v81
	s_waitcnt lgkmcnt(8)
	v_mfma_f32_32x32x16_f16 v[96:111], v[214:217], v[128:131], v[96:111]
	v_cvt_pk_f16_f32 v9, v82, v83
	v_cvt_pk_f16_f32 v12, v88, v89
	v_cvt_pk_f16_f32 v13, v90, v91
	v_cvt_pk_f16_f32 v14, v92, v93
	v_cvt_pk_f16_f32 v15, v94, v95
	v_permlane32_swap_b32_e32 v0, v2
	v_mfma_f32_32x32x16_f16 v[112:127], v[210:213], v[128:131], v[112:127]
	v_permlane32_swap_b32_e32 v1, v3
	v_permlane32_swap_b32_e32 v4, v6
	v_permlane32_swap_b32_e32 v5, v7
	v_permlane32_swap_b32_e32 v8, v10
	v_permlane32_swap_b32_e32 v9, v11
	v_permlane32_swap_b32_e32 v12, v14
	v_permlane32_swap_b32_e32 v13, v15
	s_waitcnt lgkmcnt(0)
	s_nop 0
	v_mfma_f32_32x32x16_f16 v[64:79], v[0:3], v[162:165], v[64:79]
	s_nop 2
	v_exp_f32_e32 v210, v112
	v_exp_f32_e32 v211, v113
	ds_read_b64_tr_b16 v[112:113], v184 offset:0x8200
	v_exp_f32_e32 v212, v114
	v_exp_f32_e32 v213, v115
	ds_read_b64_tr_b16 v[114:115], v184 offset:0x8a00
	ds_read_b64_tr_b16 v[162:163], v184 offset:0x9200
	v_mfma_f32_32x32x16_f16 v[64:79], v[4:7], v[166:169], v[64:79]
	ds_read_b64_tr_b16 v[164:165], v184 offset:0x9a00
	ds_read_b64_tr_b16 v[166:167], v184 offset:0xa200
	ds_read_b64_tr_b16 v[168:169], v184 offset:0xaa00
	v_mfma_f32_32x32x16_f16 v[64:79], v[8:11], v[170:173], v[64:79]
	ds_read_b64_tr_b16 v[170:171], v184 offset:0xb200
	ds_read_b64_tr_b16 v[172:173], v184 offset:0xba00
	v_mfma_f32_32x32x16_f16 v[64:79], v[12:15], v[174:177], v[64:79]
	s_waitcnt lgkmcnt(0)
	v_mfma_f32_32x32x16_f16 v[48:63], v[0:3], v[112:115], v[48:63]
	ds_read_b64_tr_b16 v[112:113], v184 offset:0x8400
	ds_read_b64_tr_b16 v[114:115], v184 offset:0x8c00
	v_exp_f32_e32 v214, v116
	v_exp_f32_e32 v215, v117
	ds_read_b64_tr_b16 v[116:117], v184 offset:0x9400
	v_exp_f32_e32 v216, v118
	v_exp_f32_e32 v217, v119
	v_mfma_f32_32x32x16_f16 v[48:63], v[4:7], v[162:165], v[48:63]
	ds_read_b64_tr_b16 v[118:119], v184 offset:0x9c00
	ds_read_b64_tr_b16 v[162:163], v184 offset:0xa400
	ds_read_b64_tr_b16 v[164:165], v184 offset:0xac00
	v_mfma_f32_32x32x16_f16 v[48:63], v[8:11], v[166:169], v[48:63]
	ds_read_b64_tr_b16 v[166:167], v184 offset:0xb400
	ds_read_b64_tr_b16 v[168:169], v184 offset:0xbc00
	v_mfma_f32_32x32x16_f16 v[48:63], v[12:15], v[170:173], v[48:63]
	s_waitcnt lgkmcnt(0)
	v_mfma_f32_32x32x16_f16 v[32:47], v[0:3], v[112:115], v[32:47]
	ds_read_b64_tr_b16 v[112:113], v184 offset:0x8600
	ds_read_b64_tr_b16 v[114:115], v184 offset:0x8e00
	v_exp_f32_e32 v218, v120
	v_exp_f32_e32 v219, v121
	v_exp_f32_e32 v220, v122
	v_exp_f32_e32 v221, v123
	v_mfma_f32_32x32x16_f16 v[32:47], v[4:7], v[116:119], v[32:47]
	ds_read_b64_tr_b16 v[116:117], v184 offset:0x9600
	ds_read_b64_tr_b16 v[118:119], v184 offset:0x9e00
	ds_read_b64_tr_b16 v[120:121], v184 offset:0xa600
	ds_read_b64_tr_b16 v[122:123], v184 offset:0xae00
	v_mfma_f32_32x32x16_f16 v[32:47], v[8:11], v[162:165], v[32:47]
	ds_read_b64_tr_b16 v[162:163], v184 offset:0xb600
	ds_read_b64_tr_b16 v[164:165], v184 offset:0xbe00
	v_mfma_f32_32x32x16_f16 v[32:47], v[12:15], v[166:169], v[32:47]
	s_waitcnt lgkmcnt(0)
	v_mfma_f32_32x32x16_f16 v[16:31], v[0:3], v[112:115], v[16:31]
	v_exp_f32_e32 v222, v124
	v_exp_f32_e32 v223, v125
	v_exp_f32_e32 v224, v126
	v_exp_f32_e32 v225, v127
	s_waitcnt vmcnt(0) lgkmcnt(0)
	s_barrier
	v_mfma_f32_32x32x16_f16 v[16:31], v[4:7], v[116:119], v[16:31]
	v_mfma_f32_32x32x16_f16 v[16:31], v[8:11], v[120:123], v[16:31]
	v_mfma_f32_32x32x16_f16 v[16:31], v[12:15], v[162:165], v[16:31]
	s_add_i32 s97, s97, 2
	s_add_i32 s1, s1, 4
	s_add_i32 s0, s0, 0x10000
	s_cmp_le_u32 s1, s99
	s_cbranch_scc1 .LBB3_3
	v_mul_i32_i24_e32 v0, -4, v160
	s_lshl_b32 s0, s4, 6
	v_subrev_u32_e32 v209, s0, v0
	s_cmp_gt_u32 s97, s99
	v_add_u32_e32 v160, v209, v161
	s_cbranch_scc1 .LBB3_18
	s_cmp_lt_u32 s97, s99
	s_cselect_b64 s[6:7], -1, 0
	s_cmp_ge_u32 s97, s99
	s_cselect_b64 s[4:5], -1, 0
	ds_read_b128 v[80:83], v190 offset:32768
	ds_read_b128 v[112:115], v190 offset:40960
	s_and_b64 vcc, exec, s[4:5]
	s_waitcnt lgkmcnt(1)
	v_mfma_f32_32x32x16_f16 v[0:15], v[80:83], v[156:159], -0.5
	s_waitcnt lgkmcnt(0)
	v_mfma_f32_32x32x16_f16 v[80:95], v[112:115], v[156:159], -0.5
	s_cbranch_vccnz .LBB3_7
	s_lshl_b32 s0, s97, 15
	s_add_i32 s0, s0, 0x8000
	s_mov_b32 m0, s86
	s_nop 0
	buffer_load_dwordx4 v191, s[68:71], s0 offen lds

.LBB3_44:
	s_mov_b32 s5, s99
	s_mov_b32 m0, s86
	s_add_i32 s6, s4, 0xffff2000
	ds_read_b128 v[0:3], v190 offset:32768
	ds_read_b128 v[82:85], v190 offset:40960
	buffer_load_dwordx4 v191, s[68:71], s6 offen lds
	ds_read_b128 v[4:7], v189 offset:32768
	ds_read_b128 v[86:89], v189 offset:40960
	s_add_i32 s7, s4, 0xffff4000
	s_mov_b32 m0, s85
	s_waitcnt lgkmcnt(3)
	v_mfma_f32_32x32x16_f16 v[112:127], v[0:3], v[156:159], -0.5
	s_add_i32 s8, s4, 0xffff6000
	buffer_load_dwordx4 v191, s[68:71], s7 offen lds
	s_waitcnt lgkmcnt(1)
	v_mfma_f32_32x32x16_f16 v[112:127], v[4:7], v[152:155], v[112:127]
	v_mfma_f32_32x32x16_f16 v[0:15], v[82:85], v[156:159], -0.5
	ds_read_b128 v[82:85], v188 offset:32768
	s_mov_b32 m0, s84
	s_add_i32 s9, s4, 0xffff8000
	s_add_i32 s10, s4, 0xfffea000
	v_add_f32_e32 v81, 0, v169
	v_add_f32_e32 v81, v170, v81
	s_waitcnt lgkmcnt(1)
	v_mfma_f32_32x32x16_f16 v[0:15], v[86:89], v[152:155], v[0:15]
	ds_read_b128 v[86:89], v188 offset:40960
	buffer_load_dwordx4 v191, s[68:71], s8 offen lds
	s_mov_b32 m0, s83
	v_add_f32_e32 v81, v171, v81
	v_add_f32_e32 v81, v172, v81
	v_add_f32_e32 v81, v173, v81
	v_add_f32_e32 v81, v174, v81
	s_waitcnt lgkmcnt(1)
	v_mfma_f32_32x32x16_f16 v[112:127], v[82:85], v[148:151], v[112:127]
	ds_read_b128 v[82:85], v187 offset:32768
	ds_read_b128 v[90:93], v187 offset:40960
	buffer_load_dwordx4 v191, s[68:71], s9 offen lds
	s_mov_b32 m0, s90
	ds_read_b128 v[160:163], v190 offset:32896
	ds_read_b128 v[164:167], v190 offset:41088
	buffer_load_dwordx4 v186, s[72:75], s10 offen lds
	s_add_i32 s10, s4, 0xfffec000
	s_mov_b32 m0, s89
	s_waitcnt lgkmcnt(4)
	v_mfma_f32_32x32x16_f16 v[0:15], v[86:89], v[148:151], v[0:15]
	ds_read_b128 v[86:89], v189 offset:32896
	ds_read_b128 v[192:195], v189 offset:41088
	buffer_load_dwordx4 v186, s[72:75], s10 offen lds
	s_add_i32 s10, s4, 0xfffee000
	s_mov_b32 m0, s88
	v_add_f32_e32 v81, v175, v81
	v_add_f32_e32 v81, v176, v81
	v_add_f32_e32 v81, v177, v81
	s_waitcnt lgkmcnt(5)
	v_mfma_f32_32x32x16_f16 v[112:127], v[82:85], v[144:147], v[112:127]
	ds_read_b128 v[82:85], v188 offset:32896
	ds_read_b128 v[196:199], v188 offset:41088
	buffer_load_dwordx4 v186, s[72:75], s10 offen lds
	s_add_i32 s10, s4, 0xffff0000
	s_mov_b32 m0, s87
	ds_read_b128 v[200:203], v187 offset:32896
	ds_read_b128 v[204:207], v187 offset:41088
	buffer_load_dwordx4 v186, s[72:75], s10 offen lds
	v_add_f32_e32 v81, v178, v81
	s_waitcnt lgkmcnt(8)
	v_mfma_f32_32x32x16_f16 v[0:15], v[90:93], v[144:147], v[0:15]
	v_add_f32_e32 v81, v179, v81
	v_add_f32_e32 v81, v180, v81
	v_exp_f32_e32 v90, v96
	v_add_f32_e32 v81, v181, v81
	v_exp_f32_e32 v91, v97
	v_add_f32_e32 v81, v182, v81
	v_exp_f32_e32 v92, v98
	s_waitcnt lgkmcnt(6)
	v_mfma_f32_32x32x16_f16 v[0:15], v[164:167], v[140:143], v[0:15]
	v_add_f32_e32 v81, v183, v81
	v_exp_f32_e32 v93, v99
	v_add_f32_e32 v81, v185, v81
	v_exp_f32_e32 v94, v100
	v_add_f32_e32 v81, v90, v81
	v_exp_f32_e32 v95, v101
	v_add_f32_e32 v81, v91, v81
	v_mfma_f32_32x32x16_f16 v[112:127], v[160:163], v[140:143], v[112:127]
	v_exp_f32_e32 v96, v102
	v_add_f32_e32 v81, v92, v81
	v_exp_f32_e32 v97, v103
	v_add_f32_e32 v81, v93, v81
	v_exp_f32_e32 v98, v104
	v_add_f32_e32 v81, v94, v81
	v_exp_f32_e32 v99, v105
	s_waitcnt lgkmcnt(4)
	v_mfma_f32_32x32x16_f16 v[0:15], v[192:195], v[136:139], v[0:15]
	v_add_f32_e32 v81, v95, v81
	v_exp_f32_e32 v100, v106
	v_add_f32_e32 v81, v96, v81
	v_exp_f32_e32 v101, v107
	v_add_f32_e32 v81, v97, v81
	v_exp_f32_e32 v102, v108
	v_add_f32_e32 v81, v98, v81
	v_mfma_f32_32x32x16_f16 v[112:127], v[86:89], v[136:139], v[112:127]
	v_exp_f32_e32 v103, v109
	v_add_f32_e32 v81, v99, v81
	v_exp_f32_e32 v104, v110
	v_add_f32_e32 v81, v100, v81
	v_exp_f32_e32 v105, v111
	v_add_f32_e32 v81, v101, v81
	v_add_f32_e32 v81, v102, v81
	s_waitcnt lgkmcnt(2)
	v_mfma_f32_32x32x16_f16 v[0:15], v[196:199], v[132:135], v[0:15]
	v_add_f32_e32 v81, v103, v81
	v_add_f32_e32 v81, v104, v81
	v_add_f32_e32 v81, v105, v81
	v_cvt_pk_f16_f32 v86, v181, v182
	v_cvt_pk_f16_f32 v87, v183, v185
	v_cvt_pk_f16_f32 v88, v90, v91
	v_cvt_pk_f16_f32 v89, v92, v93
	v_mfma_f32_32x32x16_f16 v[112:127], v[82:85], v[132:135], v[112:127]
	v_mov_b32_e32 v82, v81
	s_nop 1
	v_permlane32_swap_b32_e32 v81, v82
	v_add_f32_e32 v81, v81, v82
	v_add_f32_e32 v209, v80, v81
	v_cvt_pk_f16_f32 v80, v169, v170
	v_cvt_pk_f16_f32 v82, v173, v174
	s_waitcnt lgkmcnt(0)
	v_mfma_f32_32x32x16_f16 v[0:15], v[204:207], v[128:131], v[0:15]
	v_cvt_pk_f16_f32 v81, v171, v172
	v_cvt_pk_f16_f32 v83, v175, v176
	v_permlane32_swap_b32_e32 v80, v82
	v_cvt_pk_f16_f32 v84, v177, v178
	v_cvt_pk_f16_f32 v85, v179, v180
	v_cvt_pk_f16_f32 v90, v94, v95
	v_cvt_pk_f16_f32 v91, v96, v97
	ds_read_b64_tr_b16 v[96:97], v184 offset:0
	v_cvt_pk_f16_f32 v92, v98, v99
	ds_read_b64_tr_b16 v[98:99], v184 offset:0x800
	v_cvt_pk_f16_f32 v93, v100, v101
	ds_read_b64_tr_b16 v[100:101], v184 offset:0x1000
	v_cvt_pk_f16_f32 v94, v102, v103
	ds_read_b64_tr_b16 v[102:103], v184 offset:0x1800
	v_cvt_pk_f16_f32 v95, v104, v105
	ds_read_b64_tr_b16 v[104:105], v184 offset:0x2000
	ds_read_b64_tr_b16 v[106:107], v184 offset:0x2800
	ds_read_b64_tr_b16 v[108:109], v184 offset:0x3000
	ds_read_b64_tr_b16 v[110:111], v184 offset:0x3800
	v_mfma_f32_32x32x16_f16 v[112:127], v[200:203], v[128:131], v[112:127]
	v_permlane32_swap_b32_e32 v81, v83
	v_permlane32_swap_b32_e32 v84, v86
	v_permlane32_swap_b32_e32 v85, v87
	v_permlane32_swap_b32_e32 v88, v90
	v_permlane32_swap_b32_e32 v89, v91
	v_permlane32_swap_b32_e32 v92, v94
	v_permlane32_swap_b32_e32 v93, v95
	s_waitcnt lgkmcnt(0)
	s_nop 0
	v_mfma_f32_32x32x16_f16 v[64:79], v[80:83], v[96:99], v[64:79]
	ds_read_b64_tr_b16 v[96:97], v184 offset:0x200
	ds_read_b64_tr_b16 v[98:99], v184 offset:0xa00
	s_nop 2
	v_exp_f32_e32 v208, v112
	v_exp_f32_e32 v192, v113
	v_exp_f32_e32 v193, v114
	v_exp_f32_e32 v194, v115
	v_mfma_f32_32x32x16_f16 v[64:79], v[84:87], v[100:103], v[64:79]
	ds_read_b64_tr_b16 v[100:101], v184 offset:0x1200
	ds_read_b64_tr_b16 v[102:103], v184 offset:0x1a00
	v_mfma_f32_32x32x16_f16 v[64:79], v[88:91], v[104:107], v[64:79]
	ds_read_b64_tr_b16 v[104:105], v184 offset:0x2200
	ds_read_b64_tr_b16 v[106:107], v184 offset:0x2a00
	ds_read_b64_tr_b16 v[112:113], v184 offset:0x3200
	ds_read_b64_tr_b16 v[114:115], v184 offset:0x3a00
	v_mfma_f32_32x32x16_f16 v[64:79], v[92:95], v[108:111], v[64:79]
	s_waitcnt lgkmcnt(0)
	v_mfma_f32_32x32x16_f16 v[48:63], v[80:83], v[96:99], v[48:63]
	ds_read_b64_tr_b16 v[96:97], v184 offset:0x400
	ds_read_b64_tr_b16 v[98:99], v184 offset:0xc00
	v_exp_f32_e32 v195, v116
	v_exp_f32_e32 v196, v117
	v_exp_f32_e32 v197, v118
	v_exp_f32_e32 v198, v119
	v_mfma_f32_32x32x16_f16 v[48:63], v[84:87], v[100:103], v[48:63]
	ds_read_b64_tr_b16 v[100:101], v184 offset:0x1400
	ds_read_b64_tr_b16 v[102:103], v184 offset:0x1c00
	v_mfma_f32_32x32x16_f16 v[48:63], v[88:91], v[104:107], v[48:63]
	ds_read_b64_tr_b16 v[104:105], v184 offset:0x2400
	ds_read_b64_tr_b16 v[106:107], v184 offset:0x2c00
	ds_read_b64_tr_b16 v[108:109], v184 offset:0x3400
	ds_read_b64_tr_b16 v[110:111], v184 offset:0x3c00
	v_mfma_f32_32x32x16_f16 v[48:63], v[92:95], v[112:115], v[48:63]
	s_waitcnt lgkmcnt(0)
	v_mfma_f32_32x32x16_f16 v[32:47], v[80:83], v[96:99], v[32:47]
	ds_read_b64_tr_b16 v[96:97], v184 offset:0x600
	ds_read_b64_tr_b16 v[98:99], v184 offset:0xe00
	v_exp_f32_e32 v199, v120
	v_exp_f32_e32 v200, v121
	v_exp_f32_e32 v201, v122
	v_exp_f32_e32 v202, v123
	v_mfma_f32_32x32x16_f16 v[32:47], v[84:87], v[100:103], v[32:47]
	ds_read_b64_tr_b16 v[100:101], v184 offset:0x1600
	ds_read_b64_tr_b16 v[102:103], v184 offset:0x1e00
	v_mfma_f32_32x32x16_f16 v[32:47], v[88:91], v[104:107], v[32:47]
	ds_read_b64_tr_b16 v[104:105], v184 offset:0x2600
	ds_read_b64_tr_b16 v[106:107], v184 offset:0x2e00
	ds_read_b64_tr_b16 v[112:113], v184 offset:0x3600
	ds_read_b64_tr_b16 v[114:115], v184 offset:0x3e00
	v_mfma_f32_32x32x16_f16 v[32:47], v[92:95], v[108:111], v[32:47]
	s_waitcnt lgkmcnt(0)
	v_mfma_f32_32x32x16_f16 v[16:31], v[80:83], v[96:99], v[16:31]
	v_exp_f32_e32 v203, v124
	v_exp_f32_e32 v204, v125
	v_exp_f32_e32 v205, v126
	v_exp_f32_e32 v206, v127
	s_waitcnt vmcnt(0) lgkmcnt(0)
	s_barrier
	v_mfma_f32_32x32x16_f16 v[16:31], v[84:87], v[100:103], v[16:31]
	v_mfma_f32_32x32x16_f16 v[16:31], v[88:91], v[104:107], v[16:31]
	v_mfma_f32_32x32x16_f16 v[16:31], v[92:95], v[112:115], v[16:31]
	s_mov_b32 m0, s91
	s_add_i32 s10, s4, 0xffffa000
	ds_read_b128 v[80:83], v190
	ds_read_b128 v[84:87], v190 offset:8192
	buffer_load_dwordx4 v191, s[68:71], s10 offen lds
	ds_read_b128 v[88:91], v189
	ds_read_b128 v[92:95], v189 offset:8192
	s_add_i32 s10, s4, 0xffffc000
	s_mov_b32 m0, s92
	s_waitcnt lgkmcnt(3)
	v_mfma_f32_32x32x16_f16 v[112:127], v[80:83], v[156:159], -0.5
	s_waitcnt lgkmcnt(2)
	v_mfma_f32_32x32x16_f16 v[96:111], v[84:87], v[156:159], -0.5
	v_exp_f32_e32 v0, v0
	buffer_load_dwordx4 v191, s[68:71], s10 offen lds
	ds_read_b128 v[80:83], v188
	ds_read_b128 v[84:87], v188 offset:8192
	s_waitcnt lgkmcnt(3)
	v_mfma_f32_32x32x16_f16 v[112:127], v[88:91], v[152:155], v[112:127]
	s_add_i32 s10, s4, 0xffffe000
	s_mov_b32 m0, s93
	v_exp_f32_e32 v1, v1
	buffer_load_dwordx4 v191, s[68:71], s10 offen lds
	s_mov_b32 m0, s94
	v_exp_f32_e32 v2, v2
	v_exp_f32_e32 v3, v3
	s_waitcnt lgkmcnt(2)
	v_mfma_f32_32x32x16_f16 v[96:111], v[92:95], v[152:155], v[96:111]
	v_exp_f32_e32 v4, v4
	v_exp_f32_e32 v5, v5
	v_exp_f32_e32 v6, v6
	v_exp_f32_e32 v7, v7
	v_exp_f32_e32 v8, v8
	v_exp_f32_e32 v9, v9
	v_exp_f32_e32 v10, v10
	s_waitcnt lgkmcnt(1)
	v_mfma_f32_32x32x16_f16 v[112:127], v[80:83], v[148:151], v[112:127]
	ds_read_b128 v[80:83], v187
	ds_read_b128 v[88:91], v187 offset:8192
	buffer_load_dwordx4 v191, s[68:71], s4 offen lds
	s_mov_b32 m0, s3
	ds_read_b128 v[92:95], v190 offset:128
	ds_read_b128 v[160:163], v190 offset:8320
	buffer_load_dwordx4 v186, s[72:75], s6 offen lds
	s_mov_b32 m0, s82
	v_exp_f32_e32 v11, v11
	s_waitcnt lgkmcnt(4)
	v_mfma_f32_32x32x16_f16 v[96:111], v[84:87], v[148:151], v[96:111]
	ds_read_b128 v[84:87], v189 offset:128
	ds_read_b128 v[164:167], v189 offset:8320
	buffer_load_dwordx4 v186, s[72:75], s7 offen lds
	s_mov_b32 m0, s81
	ds_read_b128 v[170:173], v188 offset:128
	ds_read_b128 v[174:177], v188 offset:8320
	buffer_load_dwordx4 v186, s[72:75], s8 offen lds
	s_mov_b32 m0, s80
	v_exp_f32_e32 v12, v12
	s_waitcnt lgkmcnt(7)
	v_mfma_f32_32x32x16_f16 v[112:127], v[80:83], v[144:147], v[112:127]
	ds_read_b128 v[80:83], v187 offset:128
	ds_read_b128 v[178:181], v187 offset:8320
	buffer_load_dwordx4 v186, s[72:75], s9 offen lds
	v_exp_f32_e32 v13, v13
	v_exp_f32_e32 v14, v14
	v_exp_f32_e32 v15, v15
	s_waitcnt lgkmcnt(8)
	v_mfma_f32_32x32x16_f16 v[96:111], v[88:91], v[144:147], v[96:111]
	v_add_f32_e32 v88, 0, v208
	v_add_f32_e32 v88, v192, v88
	v_add_f32_e32 v88, v193, v88
	v_add_f32_e32 v88, v194, v88
	v_add_f32_e32 v88, v195, v88
	v_add_f32_e32 v88, v196, v88
	v_add_f32_e32 v88, v197, v88
	s_waitcnt lgkmcnt(7)
	v_mfma_f32_32x32x16_f16 v[112:127], v[92:95], v[140:143], v[112:127]
	v_add_f32_e32 v88, v198, v88
	v_cvt_pk_f16_f32 v89, v205, v206
	v_cvt_pk_f16_f32 v90, v0, v1
	v_cvt_pk_f16_f32 v91, v2, v3
	v_cvt_pk_f16_f32 v92, v4, v5
	v_cvt_pk_f16_f32 v93, v6, v7
	s_nop 0
	v_permlane32_swap_b32_e32 v90, v92
	s_waitcnt lgkmcnt(6)
	v_mfma_f32_32x32x16_f16 v[96:111], v[160:163], v[140:143], v[96:111]
	v_cvt_pk_f16_f32 v160, v8, v9
	v_cvt_pk_f16_f32 v161, v10, v11
	v_cvt_pk_f16_f32 v162, v12, v13
	v_cvt_pk_f16_f32 v163, v14, v15
	v_permlane32_swap_b32_e32 v91, v93
	v_permlane32_swap_b32_e32 v160, v162
	s_waitcnt lgkmcnt(5)
	v_mfma_f32_32x32x16_f16 v[112:127], v[84:87], v[136:139], v[112:127]
	v_add_f32_e32 v84, v199, v88
	v_add_f32_e32 v84, v200, v84
	v_add_f32_e32 v84, v201, v84
	v_add_f32_e32 v84, v202, v84
	v_add_f32_e32 v84, v203, v84
	v_add_f32_e32 v84, v204, v84
	v_add_f32_e32 v84, v205, v84
	s_waitcnt lgkmcnt(4)
	v_mfma_f32_32x32x16_f16 v[96:111], v[164:167], v[136:139], v[96:111]
	ds_read_b64_tr_b16 v[164:165], v184 offset:0x8000
	ds_read_b64_tr_b16 v[166:167], v184 offset:0x8800
	v_add_f32_e32 v84, v206, v84
	v_add_f32_e32 v84, v0, v84
	v_add_f32_e32 v84, v1, v84
	v_add_f32_e32 v84, v2, v84
	v_add_f32_e32 v84, v3, v84
	v_add_f32_e32 v84, v4, v84
	v_add_f32_e32 v84, v5, v84
	s_waitcnt lgkmcnt(4)
	v_mfma_f32_32x32x16_f16 v[96:111], v[174:177], v[132:135], v[96:111]
	v_add_f32_e32 v84, v6, v84
	v_add_f32_e32 v84, v7, v84
	v_add_f32_e32 v84, v8, v84
	v_add_f32_e32 v84, v9, v84
	v_add_f32_e32 v84, v10, v84
	v_add_f32_e32 v84, v11, v84
	v_add_f32_e32 v84, v12, v84
	v_mfma_f32_32x32x16_f16 v[112:127], v[170:173], v[132:135], v[112:127]
	ds_read_b64_tr_b16 v[170:171], v184 offset:0x9000
	ds_read_b64_tr_b16 v[172:173], v184 offset:0x9800
	ds_read_b64_tr_b16 v[174:175], v184 offset:0xa000
	ds_read_b64_tr_b16 v[176:177], v184 offset:0xa800
	v_add_f32_e32 v84, v13, v84
	v_add_f32_e32 v84, v14, v84
	v_add_f32_e32 v84, v15, v84
	v_mov_b32_e32 v85, v84
	s_nop 1
	v_permlane32_swap_b32_e32 v84, v85
	v_add_f32_e32 v84, v84, v85
	s_waitcnt lgkmcnt(6)
	v_mfma_f32_32x32x16_f16 v[96:111], v[178:181], v[128:131], v[96:111]
	ds_read_b64_tr_b16 v[178:179], v184 offset:0xb000
	ds_read_b64_tr_b16 v[180:181], v184 offset:0xb800
	v_cvt_pk_f16_f32 v85, v197, v198
	v_cvt_pk_f16_f32 v86, v199, v200
	v_cvt_pk_f16_f32 v87, v201, v202
	v_cvt_pk_f16_f32 v88, v203, v204
	s_nop 1
	v_permlane32_swap_b32_e32 v86, v88
	v_permlane32_swap_b32_e32 v87, v89
	v_mfma_f32_32x32x16_f16 v[112:127], v[80:83], v[128:131], v[112:127]
	v_add_f32_e32 v80, v209, v84
	v_cvt_pk_f16_f32 v82, v208, v192
	v_cvt_pk_f16_f32 v83, v193, v194
	v_cvt_pk_f16_f32 v84, v195, v196
	s_nop 1
	v_permlane32_swap_b32_e32 v82, v84
	v_permlane32_swap_b32_e32 v83, v85
	v_permlane32_swap_b32_e32 v161, v163
	s_waitcnt lgkmcnt(0)
	s_nop 0
	v_mfma_f32_32x32x16_f16 v[64:79], v[82:85], v[164:167], v[64:79]
	s_nop 0
	v_exp_f32_e32 v169, v112
	v_mfma_f32_32x32x16_f16 v[64:79], v[86:89], v[170:173], v[64:79]
	v_exp_f32_e32 v170, v113
	ds_read_b64_tr_b16 v[112:113], v184 offset:0x8200
	v_exp_f32_e32 v171, v114
	v_exp_f32_e32 v172, v115
	ds_read_b64_tr_b16 v[114:115], v184 offset:0x8a00
	ds_read_b64_tr_b16 v[164:165], v184 offset:0x9200
	ds_read_b64_tr_b16 v[166:167], v184 offset:0x9a00
	v_mfma_f32_32x32x16_f16 v[64:79], v[90:93], v[174:177], v[64:79]
	ds_read_b64_tr_b16 v[210:211], v184 offset:0xa200
	ds_read_b64_tr_b16 v[212:213], v184 offset:0xaa00
	ds_read_b64_tr_b16 v[214:215], v184 offset:0xb200
	ds_read_b64_tr_b16 v[216:217], v184 offset:0xba00
	v_mfma_f32_32x32x16_f16 v[64:79], v[160:163], v[178:181], v[64:79]
	s_waitcnt lgkmcnt(0)
	v_mfma_f32_32x32x16_f16 v[48:63], v[82:85], v[112:115], v[48:63]
	ds_read_b64_tr_b16 v[112:113], v184 offset:0x8400
	ds_read_b64_tr_b16 v[114:115], v184 offset:0x8c00
	v_exp_f32_e32 v173, v116
	v_exp_f32_e32 v174, v117
	ds_read_b64_tr_b16 v[116:117], v184 offset:0x9400
	v_exp_f32_e32 v175, v118
	v_exp_f32_e32 v176, v119
	v_mfma_f32_32x32x16_f16 v[48:63], v[86:89], v[164:167], v[48:63]
	ds_read_b64_tr_b16 v[118:119], v184 offset:0x9c00
	ds_read_b64_tr_b16 v[164:165], v184 offset:0xa400
	ds_read_b64_tr_b16 v[166:167], v184 offset:0xac00
	v_mfma_f32_32x32x16_f16 v[48:63], v[90:93], v[210:213], v[48:63]
	ds_read_b64_tr_b16 v[210:211], v184 offset:0xb400
	ds_read_b64_tr_b16 v[212:213], v184 offset:0xbc00
	v_mfma_f32_32x32x16_f16 v[48:63], v[160:163], v[214:217], v[48:63]
	s_waitcnt lgkmcnt(0)
	v_mfma_f32_32x32x16_f16 v[32:47], v[82:85], v[112:115], v[32:47]
	ds_read_b64_tr_b16 v[112:113], v184 offset:0x8600
	ds_read_b64_tr_b16 v[114:115], v184 offset:0x8e00
	v_exp_f32_e32 v177, v120
	v_exp_f32_e32 v178, v121
	v_exp_f32_e32 v179, v122
	v_exp_f32_e32 v180, v123
	v_mfma_f32_32x32x16_f16 v[32:47], v[86:89], v[116:119], v[32:47]
	ds_read_b64_tr_b16 v[116:117], v184 offset:0x9600
	ds_read_b64_tr_b16 v[118:119], v184 offset:0x9e00
	ds_read_b64_tr_b16 v[120:121], v184 offset:0xa600
	ds_read_b64_tr_b16 v[122:123], v184 offset:0xae00
	v_mfma_f32_32x32x16_f16 v[32:47], v[90:93], v[164:167], v[32:47]
	ds_read_b64_tr_b16 v[164:165], v184 offset:0xb600
	ds_read_b64_tr_b16 v[166:167], v184 offset:0xbe00
	v_mfma_f32_32x32x16_f16 v[32:47], v[160:163], v[210:213], v[32:47]
	s_waitcnt lgkmcnt(0)
	v_mfma_f32_32x32x16_f16 v[16:31], v[82:85], v[112:115], v[16:31]
	v_exp_f32_e32 v181, v124
	v_exp_f32_e32 v182, v125
	v_exp_f32_e32 v183, v126
	v_exp_f32_e32 v185, v127
	s_waitcnt vmcnt(0) lgkmcnt(0)
	s_barrier
	v_mfma_f32_32x32x16_f16 v[16:31], v[86:89], v[116:119], v[16:31]
	v_mfma_f32_32x32x16_f16 v[16:31], v[90:93], v[120:123], v[16:31]
	v_mfma_f32_32x32x16_f16 v[16:31], v[160:163], v[164:167], v[16:31]
	s_add_i32 s99, s99, 2
	s_add_i32 s4, s4, 0x10000
	s_add_i32 s5, s5, 4
	s_cmp_le_u32 s5, s33
	s_cbranch_scc1 .LBB3_44
	s_cmp_gt_u32 s99, s33
	s_cbranch_scc0 .LBB3_47
	s_branch .LBB3_60
